# speedup vs baseline: 1.0065x; 1.0065x over previous
.LBB0_19:
	s_load_dwordx2 s[4:5], s[0:1], 0x20
	v_lshl_or_b32 v0, s2, 10, v0
	v_add_u32_e32 v0, 0xfffa0000, v0
	s_mov_b32 s0, 0
	v_ashrrev_i32_e32 v1, 31, v0
	s_waitcnt lgkmcnt(0)
	v_lshl_add_u64 v[0:1], v[0:1], 4, s[4:5]
	s_mov_b32 s2, s0
	s_mov_b32 s3, s0
	s_mov_b32 s1, s0
	v_mov_b64_e32 v[6:7], s[2:3]
	v_add_co_u32_e32 v2, vcc, 0x1000, v0
	v_mov_b64_e32 v[4:5], s[0:1]
	s_nop 0
	v_addc_co_u32_e32 v3, vcc, 0, v1, vcc
	global_store_dwordx4 v[2:3], v[4:7], off sc0 sc1
	v_add_co_u32_e32 v2, vcc, 0x2000, v0
	global_store_dwordx4 v[0:1], v[4:7], off sc0 sc1
	s_nop 0
	v_addc_co_u32_e32 v3, vcc, 0, v1, vcc
	v_add_co_u32_e32 v0, vcc, 0x3000, v0
	global_store_dwordx4 v[2:3], v[4:7], off sc0 sc1
	s_nop 0
	v_addc_co_u32_e32 v1, vcc, 0, v1, vcc
	global_store_dwordx4 v[0:1], v[4:7], off sc0 sc1
	s_endpgm

.LBB1_21:
	s_or_b64 exec, exec, s[4:5]
	s_lshr_b32 s4, s18, 16
	v_cvt_f32_u32_e32 v3, s4
	v_lshlrev_b64 v[8:9], 11, v[6:7]
	v_lshl_add_u64 v[8:9], s[16:17], 0, v[8:9]
	s_and_b32 s10, s18, 0xffff
	v_div_scale_f32 v4, s[4:5], v3, v3, 1.0
	v_rcp_f32_e32 v12, v4
	v_div_scale_f32 v13, vcc, 1.0, v3, 1.0
	v_readlane_b32 s4, v16, 0
	v_fma_f32 v17, -v4, v12, 1.0
	v_fmac_f32_e32 v12, v17, v12
	v_mul_f32_e32 v17, v13, v12
	v_fma_f32 v18, -v4, v17, v13
	v_fmac_f32_e32 v17, v18, v12
	v_fma_f32 v4, -v4, v17, v13
	v_div_fmas_f32 v4, v4, v12, v17
	v_readlane_b32 s5, v16, 1
	v_div_fixup_f32 v4, v4, v3, 1.0
	v_mov_b32_e32 v12, s4
	v_mov_b32_e32 v3, s5
	v_cmp_gt_u32_e32 vcc, 32, v2
	s_nop 1
	v_cndmask_b32_e32 v3, v3, v12, vcc
	v_and_b32_e32 v3, v3, v15
	v_cmp_ne_u32_e64 s[4:5], 0, v3
	v_mov_b32_e32 v3, 0
	v_lshl_add_u64 v[8:9], v[2:3], 2, v[8:9]
	v_cndmask_b32_e64 v12, 0, v4, s[4:5]
	v_readlane_b32 s4, v16, 2
	v_readlane_b32 s5, v16, 3
	global_store_dword v[8:9], v12, off sc0 sc1
	v_mov_b32_e32 v13, s4
	v_mov_b32_e32 v12, s5
	v_cndmask_b32_e32 v12, v12, v13, vcc
	v_and_b32_e32 v12, v12, v15
	v_cmp_ne_u32_e64 s[4:5], 0, v12
	s_nop 1
	v_cndmask_b32_e64 v12, 0, v4, s[4:5]
	v_readlane_b32 s4, v16, 4
	v_readlane_b32 s5, v16, 5
	global_store_dword v[8:9], v12, off offset:256 sc0 sc1
	v_mov_b32_e32 v13, s4
	v_mov_b32_e32 v12, s5
	v_cndmask_b32_e32 v12, v12, v13, vcc
	v_and_b32_e32 v12, v12, v15
	v_cmp_ne_u32_e64 s[4:5], 0, v12
	s_nop 1
	v_cndmask_b32_e64 v12, 0, v4, s[4:5]
	v_readlane_b32 s4, v16, 6
	v_readlane_b32 s5, v16, 7
	global_store_dword v[8:9], v12, off offset:512 sc0 sc1
	v_mov_b32_e32 v13, s4
	v_mov_b32_e32 v12, s5
	v_cndmask_b32_e32 v12, v12, v13, vcc
	v_and_b32_e32 v12, v12, v15
	v_cmp_ne_u32_e64 s[4:5], 0, v12
	s_nop 1
	v_cndmask_b32_e64 v12, 0, v4, s[4:5]
	v_readlane_b32 s4, v16, 8
	v_readlane_b32 s5, v16, 9
	global_store_dword v[8:9], v12, off offset:768 sc0 sc1
	v_mov_b32_e32 v13, s4
	v_mov_b32_e32 v12, s5
	v_cndmask_b32_e32 v12, v12, v13, vcc
	v_and_b32_e32 v12, v12, v15
	v_cmp_ne_u32_e64 s[4:5], 0, v12
	s_nop 1
	v_cndmask_b32_e64 v12, 0, v4, s[4:5]
	v_readlane_b32 s4, v16, 10
	v_readlane_b32 s5, v16, 11
	global_store_dword v[8:9], v12, off offset:1024 sc0 sc1
	v_mov_b32_e32 v13, s4
	v_mov_b32_e32 v12, s5
	v_cndmask_b32_e32 v12, v12, v13, vcc
	v_and_b32_e32 v12, v12, v15
	v_cmp_ne_u32_e64 s[4:5], 0, v12
	s_nop 1
	v_cndmask_b32_e64 v12, 0, v4, s[4:5]
	v_readlane_b32 s4, v16, 12
	v_readlane_b32 s5, v16, 13
	global_store_dword v[8:9], v12, off offset:1280 sc0 sc1
	v_mov_b32_e32 v13, s4
	v_mov_b32_e32 v12, s5
	v_cndmask_b32_e32 v12, v12, v13, vcc
	v_and_b32_e32 v12, v12, v15
	v_cmp_ne_u32_e64 s[4:5], 0, v12
	s_nop 1
	v_cndmask_b32_e64 v12, 0, v4, s[4:5]
	v_readlane_b32 s4, v16, 14
	v_readlane_b32 s5, v16, 15
	global_store_dword v[8:9], v12, off offset:1536 sc0 sc1
	v_mov_b32_e32 v13, s4
	v_mov_b32_e32 v12, s5
	v_cndmask_b32_e32 v12, v12, v13, vcc
	v_and_b32_e32 v12, v12, v15
	v_cmp_ne_u32_e32 vcc, 0, v12
	v_cmp_le_u32_e64 s[4:5], s10, v2
	s_nop 0
	v_cndmask_b32_e32 v12, 0, v4, vcc
	v_cmp_gt_u32_e32 vcc, 24, v2
	s_and_b64 s[14:15], vcc, s[4:5]
	global_store_dword v[8:9], v12, off offset:1792 sc0 sc1
	s_and_saveexec_b64 s[4:5], s[14:15]
	s_cbranch_execz .LBB1_23
	v_mad_u64_u32 v[8:9], s[8:9], v6, 48, s[8:9]
	v_mad_u32_u24 v9, v7, 48, v9
	v_lshl_add_u64 v[8:9], v[2:3], 1, v[8:9]
	v_mov_b32_e32 v3, 0x2000
	global_store_short v[8:9], v3, off

.Lchain_done:
.LBB2_44:
	v_mov_b32_e32 v0, 0x10040
	v_lshl_or_b32 v54, v1, 4, v0
	v_lshl_add_u32 v0, v110, 6, v54
	v_add_u32_e32 v55, 0x4c, v67
	s_waitcnt vmcnt(8)
	ds_write_b128 v0, v[34:37]
	s_waitcnt lgkmcnt(0)
	s_barrier
	ds_read2st64_b32 v[0:1], v55 offset0:224 offset1:228
	s_add_u32 s0, s16, s18
	s_addc_u32 s1, s17, s19
	v_lshl_add_u64 v[50:51], v[98:99], 4, s[0:1]
	v_mul_u32_u24_e32 v38, 0xc00, v110
	s_waitcnt lgkmcnt(0)
	v_lshrrev_b32_e32 v0, 24, v0
	v_lshl_add_u32 v0, v0, 6, v54
	v_mov_b32_e32 v39, 0
	ds_read_b128 v[34:37], v66
	v_lshl_add_u64 v[52:53], v[50:51], 0, v[38:39]
	ds_read_b128 v[38:41], v0
	ds_read_b128 v[42:45], v66 offset:1024
	v_lshrrev_b32_e32 v0, 24, v1
	v_lshl_add_u32 v0, v0, 6, v54
	ds_read_b128 v[46:49], v0
	s_waitcnt vmcnt(7) lgkmcnt(3)
	v_pk_add_f32 v[30:31], v[34:35], v[30:31]
	v_pk_add_f32 v[0:1], v[36:37], v[32:33]
	s_waitcnt vmcnt(6) lgkmcnt(1)
	v_pk_add_f32 v[26:27], v[42:43], v[26:27]
	v_pk_add_f32 v[28:29], v[44:45], v[28:29]
	v_pk_add_f32 v[30:31], v[30:31], v[38:39]
	v_pk_add_f32 v[32:33], v[0:1], v[40:41]
	v_lshl_add_u64 v[0:1], v[50:51], 0, v[102:103]
	s_waitcnt lgkmcnt(0)
	v_pk_add_f32 v[26:27], v[26:27], v[46:47]
	ds_read2st64_b32 v[38:39], v55 offset0:232 offset1:236
	v_pk_add_f32 v[28:29], v[28:29], v[48:49]
	global_store_dwordx4 v[52:53], v[30:33], off sc0 sc1
	global_store_dwordx4 v[0:1], v[26:29], off sc0 sc1
	ds_read_b128 v[26:29], v66 offset:2048
	s_waitcnt lgkmcnt(1)
	v_lshrrev_b32_e32 v30, 24, v38
	v_lshl_add_u32 v30, v30, 6, v54
	ds_read_b128 v[30:33], v30
	ds_read_b128 v[34:37], v66 offset:3072
	s_mov_b32 s0, 0x30000
	s_waitcnt vmcnt(7) lgkmcnt(2)
	v_pk_add_f32 v[22:23], v[26:27], v[22:23]
	v_lshrrev_b32_e32 v26, 24, v39
	v_lshl_add_u32 v26, v26, 6, v54
	ds_read_b128 v[38:41], v26
	v_add_co_u32_e32 v26, vcc, s0, v0
	s_mov_b32 s0, 0x60000
	s_nop 0
	v_addc_co_u32_e32 v27, vcc, 0, v1, vcc
	s_waitcnt lgkmcnt(2)
	v_pk_add_f32 v[22:23], v[22:23], v[30:31]
	s_waitcnt vmcnt(6) lgkmcnt(1)
	v_pk_add_f32 v[18:19], v[34:35], v[18:19]
	v_pk_add_f32 v[20:21], v[36:37], v[20:21]
	ds_read2st64_b32 v[30:31], v55 offset0:240 offset1:244
	v_add_co_u32_e32 v0, vcc, s0, v0
	s_waitcnt lgkmcnt(1)
	v_pk_add_f32 v[18:19], v[18:19], v[38:39]
	v_pk_add_f32 v[20:21], v[20:21], v[40:41]
	v_addc_co_u32_e32 v1, vcc, 0, v1, vcc
	global_store_dwordx4 v[0:1], v[18:21], off sc0 sc1
	ds_read_b128 v[18:21], v66 offset:4096
	v_pk_add_f32 v[24:25], v[28:29], v[24:25]
	s_waitcnt lgkmcnt(1)
	v_lshrrev_b32_e32 v0, 24, v30
	v_pk_add_f32 v[24:25], v[24:25], v[32:33]
	global_store_dwordx4 v[26:27], v[22:25], off sc0 sc1
	v_lshl_add_u32 v0, v0, 6, v54
	ds_read_b128 v[22:25], v0
	ds_read_b128 v[26:29], v66 offset:5120
	s_waitcnt vmcnt(7) lgkmcnt(2)
	v_pk_add_f32 v[0:1], v[18:19], v[14:15]
	v_lshrrev_b32_e32 v14, 24, v31
	v_lshl_add_u32 v14, v14, 6, v54
	ds_read_b128 v[30:33], v14
	s_waitcnt lgkmcnt(2)
	v_pk_add_f32 v[14:15], v[0:1], v[22:23]
	v_pk_add_f32 v[0:1], v[20:21], v[16:17]
	s_mov_b32 s0, 0xc0000
	v_pk_add_f32 v[16:17], v[0:1], v[24:25]
	v_add_co_u32_e32 v0, vcc, s0, v52
	s_waitcnt vmcnt(6) lgkmcnt(1)
	v_pk_add_f32 v[10:11], v[26:27], v[10:11]
	v_addc_co_u32_e32 v1, vcc, 0, v53, vcc
	v_pk_add_f32 v[12:13], v[28:29], v[12:13]
	global_store_dwordx4 v[0:1], v[14:17], off sc0 sc1
	v_lshl_add_u64 v[0:1], v[50:51], 0, v[100:101]
	ds_read2st64_b32 v[22:23], v55 offset0:248 offset1:252
	s_waitcnt lgkmcnt(1)
	v_pk_add_f32 v[10:11], v[10:11], v[30:31]
	v_pk_add_f32 v[12:13], v[12:13], v[32:33]
	global_store_dwordx4 v[0:1], v[10:13], off sc0 sc1
	ds_read_b128 v[10:13], v66 offset:6144
	s_waitcnt lgkmcnt(1)
	v_lshrrev_b32_e32 v0, 24, v22
	v_lshl_add_u32 v14, v0, 6, v54
	ds_read_b128 v[14:17], v14
	ds_read_b128 v[18:21], v66 offset:7168
	v_lshl_add_u64 v[0:1], v[50:51], 0, v[96:97]
	s_waitcnt vmcnt(7) lgkmcnt(2)
	v_pk_add_f32 v[6:7], v[10:11], v[6:7]
	v_lshrrev_b32_e32 v10, 24, v23
	v_lshl_add_u32 v10, v10, 6, v54
	ds_read_b128 v[22:25], v10
	v_pk_add_f32 v[8:9], v[12:13], v[8:9]
	s_waitcnt lgkmcnt(2)
	v_pk_add_f32 v[6:7], v[6:7], v[14:15]
	v_pk_add_f32 v[8:9], v[8:9], v[16:17]
	global_store_dwordx4 v[0:1], v[6:9], off sc0 sc1
	s_waitcnt vmcnt(7) lgkmcnt(1)
	v_pk_add_f32 v[0:1], v[18:19], v[2:3]
	v_pk_add_f32 v[2:3], v[20:21], v[4:5]
	v_lshl_add_u64 v[6:7], v[50:51], 0, v[94:95]
	s_waitcnt lgkmcnt(0)
	v_pk_add_f32 v[0:1], v[0:1], v[22:23]
	v_pk_add_f32 v[2:3], v[2:3], v[24:25]
	global_store_dwordx4 v[6:7], v[0:3], off sc0 sc1
	s_endpgm
